# GEMM-in epilogue conversion: whole workgroup, first 4 units only (the long gelu / silu epilogues) instead of half a workgroup on 8 units; same tile split as v23
# baseline (speedup 1.0000x reference)
.LBB0_160:
	s_add_i32 s89, s59, -1
	s_cmp_lt_u32 s89, 4
	s_cselect_b32 s88, 1, 0
	s_cbranch_scc0 .Lp1c_skip1
	s_mul_i32 s89, s89, 200
	s_add_u32 s89, s89, s78
	s_add_u32 s89, s89, 6112
	s_cmp_lt_u32 s89, 0x2000
	s_cselect_b32 s88, 1, 0
	s_cbranch_scc0 .Lp1c_skip1
	s_lshr_b32 s90, s89, 4
	s_lshl_b32 s90, s90, 21
	s_and_b32 s91, s89, 15
	s_lshl_b32 s92, s91, 10
	s_or_b32 s90, s90, s92
	s_lshl_b32 s92, s57, 7
	s_or_b32 s90, s90, s92
	s_add_u32 s84, s82, s90
	s_addc_u32 s85, s83, 0
	s_lshr_b32 s90, s89, 8
	s_lshl_b32 s90, s90, 23
	s_lshl_b32 s91, s91, 19
	s_or_b32 s90, s90, s91
	s_bfe_u32 s91, s89, 0x40004
	s_lshl_b32 s91, s91, 7
	s_or_b32 s90, s90, s91
	s_lshl_b32 s91, s57, 15
	s_or_b32 s90, s90, s91
	s_add_u32 s90, s90, 0x4ee00000
	s_add_u32 s86, s48, s90
	s_addc_u32 s87, s49, 0
	global_load_dwordx4 v[180:183], v245, s[84:85] nt
	s_add_u32 s84, s84, 0x4000
	s_addc_u32 s85, s85, 0
	global_load_dwordx4 v[184:187], v245, s[84:85] nt
	s_add_u32 s84, s84, 0x4000
	s_addc_u32 s85, s85, 0
	global_load_dwordx4 v[188:191], v245, s[84:85] nt
	s_add_u32 s84, s84, 0x4000
	s_addc_u32 s85, s85, 0
	global_load_dwordx4 v[192:195], v245, s[84:85] nt
	s_add_u32 s84, s84, 0x4000
	s_addc_u32 s85, s85, 0
	global_load_dwordx4 v[196:199], v245, s[84:85] nt
	s_add_u32 s84, s84, 0x4000
	s_addc_u32 s85, s85, 0
	global_load_dwordx4 v[200:203], v245, s[84:85] nt
	s_add_u32 s84, s84, 0x4000
	s_addc_u32 s85, s85, 0
	global_load_dwordx4 v[204:207], v245, s[84:85] nt
	s_add_u32 s84, s84, 0x4000
	s_addc_u32 s85, s85, 0
	global_load_dwordx4 v[208:211], v245, s[84:85] nt
	s_add_u32 s84, s84, 0x4000
	s_addc_u32 s85, s85, 0
	global_load_dwordx4 v[212:215], v245, s[84:85] nt
	s_add_u32 s84, s84, 0x4000
	s_addc_u32 s85, s85, 0
	global_load_dwordx4 v[216:219], v245, s[84:85] nt
	s_add_u32 s84, s84, 0x4000
	s_addc_u32 s85, s85, 0
	global_load_dwordx4 v[220:223], v245, s[84:85] nt
	s_add_u32 s84, s84, 0x4000
	s_addc_u32 s85, s85, 0
	global_load_dwordx4 v[224:227], v245, s[84:85] nt
	s_add_u32 s84, s84, 0x4000
	s_addc_u32 s85, s85, 0
	global_load_dwordx4 v[228:231], v245, s[84:85] nt
	s_add_u32 s84, s84, 0x4000
	s_addc_u32 s85, s85, 0
	global_load_dwordx4 v[232:235], v245, s[84:85] nt
	s_add_u32 s84, s84, 0x4000
	s_addc_u32 s85, s85, 0
	global_load_dwordx4 v[236:239], v245, s[84:85] nt
	s_add_u32 s84, s84, 0x4000
	s_addc_u32 s85, s85, 0
	global_load_dwordx4 v[240:243], v245, s[84:85] nt
